# v5 + GEMM loops: per-block setprio flips deleted, one static s_setprio 1 for the leading half (wr=0) per GEMM call
# baseline (speedup 1.0000x reference)
; __global__ void __launch_bounds__(NWAVES * 64, 2) mk_fwd(Args args) {
;     ...
;         { pg8::Gemm g{(const pg8::bf16_t*)F.H1Q, F.WIN, M, NPROJ, D / 2}; pg8::StaticOrder S; S.init(M, NPROJ, F.G, (int)blockIdx.x);
;           pg8::EpiQ8 E{F.PROJ, NPROJ, 2048 / 256, F.SA, F.SW, 1};
;           pg8::gemm_phase<pg8::EpiQ8, pg8::StaticOrder, PG8_ALIGN, PG8_SP2, true>(F.lds, g, S, E); }
.LBB0_270:
	s_cmp_lg_u32 s0, 0
	s_cbranch_scc1 .Lgprio_skip1
	s_setprio 1

;     __host__ __device__ bool next(int i, Unit& u) const {
;         const long L = (long)i * G + c; if (L >= nwg) return false;
;         int wgid = (int)L; { const int q = nwg / NXCD, r = nwg % NXCD, xcd = wgid % NXCD, off = wgid / NXCD; wgid = (xcd < r ? xcd * (q + 1) : r * (q + 1) + (xcd - r) * q) + off; }
; template <class Epi, class Sched, bool ALIGN_EPI = false, bool SP2 = false, bool I8 = false>
; __device__ __forceinline__ void gemm_phase(PG8_LAS unsigned char* lds, const Gemm g, const Sched& S, const Epi& E) {
;     const int tid = threadIdx.x, wid = __builtin_amdgcn_readfirstlane(tid >> 6), lane = tid & 63, wr = wid >> 2, wc = wid & 3, fr = lane & 15, fq = lane >> 4;
.LBB0_315:
	s_setprio 0
	s_cmpk_lt_i32 s58, 0x100
	s_cselect_b64 s[0:1], -1, 0
	s_cmpk_gt_i32 s58, 0xff
	v_readfirstlane_b32 s14, v0
	s_cbranch_scc1 .LBB0_321
	s_ashr_i32 s2, s58, 31
	s_lshr_b32 s2, s2, 29
	s_add_i32 s4, s58, s2
	s_and_b32 s2, s4, -8
	s_sub_i32 s5, s58, s2
	s_cmp_gt_i32 s5, -1
	s_cbranch_scc0 .LBB0_318
	s_lshl_b32 s8, s5, 5
	s_cbranch_execz .LBB0_319
	s_branch .LBB0_320

; __device__ __forceinline__ unsigned xb_add(unsigned* p, unsigned v) { return __hip_atomic_fetch_add(p, v, __ATOMIC_RELAXED, __HIP_MEMORY_SCOPE_AGENT); }
; __device__ __forceinline__ void xcd_barrier(const XcdBarrier& b) {
;     asm volatile("s_waitcnt vmcnt(0)" ::: "memory");
;     __syncthreads();
;     if (threadIdx.x == 0) {
;         unsigned* bar = b.bar;
;         __builtin_amdgcn_s_waitcnt(0);
;         unsigned nloc = b.st[0], nx = b.st[1];
;         if (nloc == 0u) { xcd_barrier_complete(bar, b.x, nloc, nx); b.st[0] = nloc; b.st[1] = nx; }
;         const unsigned old = xb_add(&bar[XB_XSUB(b.x)], 1u);
;         const unsigned gen = old / nloc;
;         if (old + 1u == (gen + 1u) * nloc) {
.LBB0_373:
	s_setprio 0
	v_readlane_b32 s0, v252, 4
	v_readlane_b32 s1, v252, 5
	s_cmp_gt_i32 s1, 3
	v_readlane_b32 s2, v252, 6
	v_readlane_b32 s3, v252, 7
	s_cselect_b64 s[0:1], -1, 0
	s_and_b64 s[2:3], s[6:7], s[0:1]
	s_andn2_b64 vcc, exec, s[2:3]
	s_cbranch_vccnz .LBB0_423
	s_waitcnt vmcnt(0)
	v_cmp_eq_u32_e32 vcc, 0, v0
	s_waitcnt lgkmcnt(0)
	s_barrier
	s_and_saveexec_b64 s[2:3], vcc
	s_cbranch_execz .LBB0_422
	v_readlane_b32 s4, v252, 38
	s_waitcnt vmcnt(0) expcnt(0) lgkmcnt(0)
	s_nop 0
	v_mov_b32_e32 v1, s4
	ds_read_b32 v3, v1
	ds_read_b32 v1, v1 offset:4
	s_waitcnt lgkmcnt(1)
	v_cmp_ne_u32_e32 vcc, 0, v3
	s_cbranch_vccnz .LBB0_390
	v_readlane_b32 s4, v252, 9
	v_readlane_b32 s5, v252, 10
	s_load_dwordx2 s[8:9], s[4:5], 0x4
	v_readlane_b32 s4, v252, 35
	v_readlane_b32 s5, v252, 36
	s_lshl_b64 s[4:5], s[4:5], 2
	v_readlane_b32 s6, v252, 33
	s_add_u32 s4, s6, s4
	v_readlane_b32 s6, v252, 34
	s_addc_u32 s5, s6, s5
	s_add_u32 s6, s4, 0x1000
	v_readlane_b32 s7, v252, 11
	s_waitcnt lgkmcnt(0)
	s_mul_i32 s20, s8, s7
	s_addc_u32 s7, s5, 0
	s_add_u32 s8, s4, 0x1100
	s_mul_i32 s20, s20, s9
	s_addc_u32 s9, s5, 0
	s_add_u32 s10, s4, 0x1200
	s_addc_u32 s11, s5, 0
	s_add_u32 s12, s4, 0x1300
	s_addc_u32 s13, s5, 0
	s_mov_b32 s21, 1
	v_mov_b32_e32 v17, 0
	s_branch .LBB0_378

; __global__ void __launch_bounds__(NWAVES * 64, 2) mk_fwd(Args args) {
;     ...
;         pg8::Gemm g{(const pg8::bf16_t*)F.YQ, (const pg8::bf16_t*)F.WO8, M, D, D / 2}; pg8::StaticOrder S; S.init(M, D, F.G, (int)blockIdx.x);
;         pg8::EpiResid2 E{(const pg8::bf16_t*)F.XB, F.MODF + MOD_GM, F.X1B, F.SSQP, D, F.SY, F.SWO};
;         pg8::gemm_phase<pg8::EpiResid2, pg8::StaticOrder, PG8_ALIGN, PG8_SP2, true>(F.lds, g, S, E);
.LBB0_964:
	s_cmp_lg_u32 s1, 0
	s_cbranch_scc1 .Lgprio_skip203
	s_setprio 1

; __device__ __forceinline__ unsigned xb_add(unsigned* p, unsigned v) { return __hip_atomic_fetch_add(p, v, __ATOMIC_RELAXED, __HIP_MEMORY_SCOPE_AGENT); }
; __device__ __forceinline__ void xcd_barrier(const XcdBarrier& b) {
;     asm volatile("s_waitcnt vmcnt(0)" ::: "memory");
;     __syncthreads();
;     if (threadIdx.x == 0) {
;         unsigned* bar = b.bar;
;         __builtin_amdgcn_s_waitcnt(0);
;         unsigned nloc = b.st[0], nx = b.st[1];
;         if (nloc == 0u) { xcd_barrier_complete(bar, b.x, nloc, nx); b.st[0] = nloc; b.st[1] = nx; }
;         const unsigned old = xb_add(&bar[XB_XSUB(b.x)], 1u);
;         const unsigned gen = old / nloc;
;         if (old + 1u == (gen + 1u) * nloc) {
.LBB0_981:
	s_setprio 0
	v_readlane_b32 s0, v252, 4
	v_readlane_b32 s1, v252, 5
	s_cmp_gt_i32 s1, 7
	v_readlane_b32 s2, v252, 6
	v_readlane_b32 s3, v252, 7
	s_cselect_b64 s[0:1], -1, 0
	s_and_b64 s[2:3], s[4:5], s[0:1]
	s_andn2_b64 vcc, exec, s[2:3]
	s_cbranch_vccnz .LBB0_1031
	s_waitcnt vmcnt(0)
	v_cmp_eq_u32_e32 vcc, 0, v0
	s_waitcnt lgkmcnt(0)
	s_barrier
	s_and_saveexec_b64 s[2:3], vcc
	s_cbranch_execz .LBB0_1030
	v_readlane_b32 s4, v252, 38
	s_waitcnt vmcnt(0) expcnt(0) lgkmcnt(0)
	s_nop 0
	v_mov_b32_e32 v1, s4
	ds_read_b32 v3, v1
	ds_read_b32 v1, v1 offset:4
	s_waitcnt lgkmcnt(1)
	v_cmp_ne_u32_e32 vcc, 0, v3
	s_cbranch_vccnz .LBB0_998
	v_readlane_b32 s4, v252, 9
	v_readlane_b32 s5, v252, 10
	s_load_dwordx2 s[8:9], s[4:5], 0x4
	v_readlane_b32 s4, v252, 35
	v_readlane_b32 s5, v252, 36
	s_lshl_b64 s[4:5], s[4:5], 2
	v_readlane_b32 s6, v252, 33
	s_add_u32 s4, s6, s4
	v_readlane_b32 s6, v252, 34
	s_addc_u32 s5, s6, s5
	s_add_u32 s6, s4, 0x1000
	v_readlane_b32 s7, v252, 11
	s_waitcnt lgkmcnt(0)
	s_mul_i32 s26, s8, s7
	s_addc_u32 s7, s5, 0
	s_add_u32 s8, s4, 0x1100
	s_mul_i32 s26, s26, s9
	s_addc_u32 s9, s5, 0
	s_add_u32 s10, s4, 0x1200
	s_addc_u32 s11, s5, 0
	s_add_u32 s12, s4, 0x1300
	s_addc_u32 s13, s5, 0
	s_mov_b32 s27, 1
	v_mov_b32_e32 v17, 0
	s_branch .LBB0_986

; __device__ __forceinline__ unsigned xb_add(unsigned* p, unsigned v) { return __hip_atomic_fetch_add(p, v, __ATOMIC_RELAXED, __HIP_MEMORY_SCOPE_AGENT); }
; __device__ __forceinline__ void xcd_barrier(const XcdBarrier& b) {
;     asm volatile("s_waitcnt vmcnt(0)" ::: "memory");
;     __syncthreads();
;     if (threadIdx.x == 0) {
;         unsigned* bar = b.bar;
;         __builtin_amdgcn_s_waitcnt(0);
;         unsigned nloc = b.st[0], nx = b.st[1];
;         if (nloc == 0u) { xcd_barrier_complete(bar, b.x, nloc, nx); b.st[0] = nloc; b.st[1] = nx; }
;         const unsigned old = xb_add(&bar[XB_XSUB(b.x)], 1u);
;         const unsigned gen = old / nloc;
;         if (old + 1u == (gen + 1u) * nloc) {
.LBB0_1151:
	s_setprio 0
	v_readlane_b32 s0, v252, 4
	v_readlane_b32 s1, v252, 5
	s_cmp_gt_i32 s1, 8
	v_readlane_b32 s2, v252, 6
	v_readlane_b32 s3, v252, 7
	s_cselect_b64 s[0:1], -1, 0
	s_and_b64 s[2:3], s[6:7], s[0:1]
	s_andn2_b64 vcc, exec, s[2:3]
	s_cbranch_vccnz .LBB0_1201
	s_waitcnt vmcnt(0)
	v_cmp_eq_u32_e32 vcc, 0, v0
	s_waitcnt lgkmcnt(0)
	s_barrier
	s_and_saveexec_b64 s[2:3], vcc
	s_cbranch_execz .LBB0_1200
	v_readlane_b32 s4, v252, 38
	s_waitcnt vmcnt(0) expcnt(0) lgkmcnt(0)
	s_nop 0
	v_mov_b32_e32 v1, s4
	ds_read_b32 v3, v1
	ds_read_b32 v1, v1 offset:4
	s_waitcnt lgkmcnt(1)
	v_cmp_ne_u32_e32 vcc, 0, v3
	s_cbranch_vccnz .LBB0_1168
	v_readlane_b32 s4, v252, 9
	v_readlane_b32 s5, v252, 10
	s_load_dwordx2 s[8:9], s[4:5], 0x4
	v_readlane_b32 s4, v252, 35
	v_readlane_b32 s5, v252, 36
	s_lshl_b64 s[4:5], s[4:5], 2
	v_readlane_b32 s6, v252, 33
	s_add_u32 s4, s6, s4
	v_readlane_b32 s6, v252, 34
	s_addc_u32 s5, s6, s5
	s_add_u32 s6, s4, 0x1000
	v_readlane_b32 s7, v252, 11
	s_waitcnt lgkmcnt(0)
	s_mul_i32 s20, s8, s7
	s_addc_u32 s7, s5, 0
	s_add_u32 s8, s4, 0x1100
	s_mul_i32 s20, s20, s9
	s_addc_u32 s9, s5, 0
	s_add_u32 s10, s4, 0x1200
	s_addc_u32 s11, s5, 0
	s_add_u32 s12, s4, 0x1300
	s_addc_u32 s13, s5, 0
	s_mov_b32 s21, 1
	v_mov_b32_e32 v17, 0
	s_branch .LBB0_1156
